# zero operand lanes for the redundant rows of the W2-dot MFMAs and for the unused k>=17 lanes of the layer-0 weights
# baseline (speedup 1.0000x reference)
_Z16pdag_main_kernelPKfS0_S0_PKDv8_DF16_S3_S0_PKDF16_S5_S0_Pf:
	s_load_dwordx8 s[4:11], s[0:1], 0x0
	s_load_dwordx8 s[12:19], s[0:1], 0x20
	s_lshl_b32 s2, s2, 6
	s_ashr_i32 s3, s2, 31
	s_lshl_b64 s[24:25], s[2:3], 6
	v_mov_b32_e32 v136, 0
	s_waitcnt lgkmcnt(0)
	s_add_u32 s4, s4, s24
	s_addc_u32 s5, s5, s25
	v_lshlrev_b32_e32 v146, 2, v0
	v_lshlrev_b32_e32 v172, 4, v0
	v_mov_b32_e32 v173, v136
	global_load_dword v174, v146, s[4:5]
	global_load_dword v175, v146, s[4:5] offset:2048
	v_lshl_add_u64 v[2:3], s[14:15], 0, v[172:173]
	s_movk_i32 s4, 0x2000
	v_add_co_u32_e32 v4, vcc, s4, v2
	s_movk_i32 s5, 0x4000
	s_nop 0
	v_addc_co_u32_e32 v5, vcc, 0, v3, vcc
	v_add_co_u32_e32 v6, vcc, s5, v2
	s_movk_i32 s5, 0x6000
	s_nop 0
	v_addc_co_u32_e32 v7, vcc, 0, v3, vcc
	v_add_co_u32_e32 v2, vcc, s5, v2
	v_and_b32_e32 v1, 15, v0
	s_nop 0
	v_addc_co_u32_e32 v3, vcc, 0, v3, vcc
	global_load_dwordx4 v[148:151], v[4:5], off
	global_load_dwordx4 v[152:155], v[6:7], off
	global_load_dwordx4 v[156:159], v[2:3], off
	v_lshl_add_u64 v[2:3], s[16:17], 0, v[172:173]
	v_or_b32_e32 v10, s2, v1
	v_add_co_u32_e32 v2, vcc, s4, v2
	v_or_b32_e32 v12, 16, v10
	s_nop 0
	v_addc_co_u32_e32 v3, vcc, 0, v3, vcc
	v_ashrrev_i32_e32 v11, 31, v10
	v_mad_i64_i32 v[6:7], s[4:5], v10, 40, s[6:7]
	v_ashrrev_i32_e32 v13, 31, v12
	global_load_dwordx4 v[160:163], v172, s[14:15]
	global_load_dwordx4 v[164:167], v172, s[16:17]
	global_load_dwordx4 v[168:171], v[2:3], off
	global_load_dwordx2 v[144:145], v[6:7], off offset:32
	s_nop 0
	global_load_dwordx4 v[2:5], v[6:7], off offset:16
	global_load_dwordx4 v[126:129], v[6:7], off
	v_lshl_add_u64 v[6:7], v[10:11], 4, s[8:9]
	v_mad_i64_i32 v[14:15], s[4:5], v12, 40, s[6:7]
	v_lshl_add_u64 v[12:13], v[12:13], 4, s[8:9]
	global_load_dwordx4 v[122:125], v[6:7], off
	global_load_dwordx2 v[142:143], v[14:15], off offset:32
	s_nop 0
	global_load_dwordx4 v[6:9], v[14:15], off offset:16
	global_load_dwordx4 v[118:121], v[14:15], off
	global_load_dwordx4 v[114:117], v[12:13], off
	v_or_b32_e32 v12, 32, v10
	v_ashrrev_i32_e32 v13, 31, v12
	v_readfirstlane_b32 s22, v0
	v_mad_i64_i32 v[18:19], s[4:5], v12, 40, s[6:7]
	v_lshl_add_u64 v[12:13], v[12:13], 4, s[8:9]
	v_or_b32_e32 v10, 48, v10
	s_mov_b32 s21, 0
	s_lshr_b32 s20, s22, 6
	global_load_dwordx2 v[140:141], v[18:19], off offset:32
	global_load_dwordx4 v[14:17], v[18:19], off offset:16
	global_load_dwordx4 v[110:113], v[18:19], off
	global_load_dwordx4 v[106:109], v[12:13], off
	v_ashrrev_i32_e32 v11, 31, v10
	v_mad_i64_i32 v[12:13], s[4:5], v10, 40, s[6:7]
	v_lshl_add_u64 v[10:11], v[10:11], 4, s[8:9]
	s_lshl_b64 s[4:5], s[20:21], 16
	global_load_dwordx2 v[138:139], v[12:13], off offset:32
	global_load_dwordx4 v[26:29], v[12:13], off offset:16
	global_load_dwordx4 v[102:105], v[12:13], off
	global_load_dwordx4 v[98:101], v[10:11], off
	s_add_u32 s4, s12, s4
	v_and_b32_e32 v10, 63, v0
	s_addc_u32 s5, s13, s5
	v_lshlrev_b32_e32 v130, 4, v10
	s_lshl_b64 s[6:7], s[20:21], 7
	global_load_dwordx4 v[30:33], v130, s[4:5]
	global_load_dwordx4 v[22:25], v130, s[4:5] offset:1024
	global_load_dwordx4 v[18:21], v130, s[4:5] offset:2048
	global_load_dwordx4 v[10:13], v130, s[4:5] offset:3072
	s_add_u32 s8, s18, s6
	s_addc_u32 s9, s19, s7
	v_lshlrev_b32_e32 v132, 3, v1
	global_load_dwordx2 v[134:135], v132, s[8:9]
	s_load_dwordx4 s[12:15], s[0:1], 0x40
	v_and_b32_e32 v137, 63, v0
	v_mov_b32_e32 v131, v136
	v_mov_b32_e32 v133, v136
	v_lshlrev_b32_e32 v34, 4, v137
	s_mov_b32 s19, 0x20000
	s_mov_b32 s18, 0x880000
	s_and_b32 s17, s11, 0xffff
	s_mov_b32 s16, s10
	v_lshl_or_b32 v147, s20, 12, v34
	s_lshl_b32 s55, s20, 1
	s_add_i32 s56, s55, 0
	s_and_b32 s56, s56, 15
	s_lshl_b32 s60, s56, 15
	s_add_i32 s56, s55, 1
	s_and_b32 s56, s56, 15
	s_lshl_b32 s61, s56, 15
	s_add_i32 s56, s55, 2
	s_and_b32 s56, s56, 15
	s_lshl_b32 s62, s56, 15
	s_add_i32 s56, s55, 3
	s_and_b32 s56, s56, 15
	s_lshl_b32 s63, s56, 15
	s_add_i32 s56, s55, 4
	s_and_b32 s56, s56, 15
	s_lshl_b32 s56, s56, 15
	s_add_i32 s34, s56, 0xfff68000
	s_add_i32 s56, s55, 5
	s_and_b32 s56, s56, 15
	s_lshl_b32 s56, s56, 15
	s_add_i32 s35, s56, 0xfff68000
	s_add_i32 s56, s55, 6
	s_and_b32 s56, s56, 15
	s_lshl_b32 s56, s56, 15
	s_add_i32 s36, s56, 0xfff68000
	s_add_i32 s56, s55, 7
	s_and_b32 s56, s56, 15
	s_lshl_b32 s56, s56, 15
	s_add_i32 s37, s56, 0xfff68000
	s_add_i32 s56, s55, 8
	s_and_b32 s56, s56, 15
	s_lshl_b32 s56, s56, 15
	s_add_i32 s38, s56, 0xfff68000
	s_add_i32 s56, s55, 9
	s_and_b32 s56, s56, 15
	s_lshl_b32 s56, s56, 15
	s_add_i32 s39, s56, 0xfff68000
	s_add_i32 s56, s55, 10
	s_and_b32 s56, s56, 15
	s_lshl_b32 s56, s56, 15
	s_add_i32 s40, s56, 0xfff68000
	s_add_i32 s56, s55, 11
	s_and_b32 s56, s56, 15
	s_lshl_b32 s56, s56, 15
	s_add_i32 s41, s56, 0xfff68000
	s_add_i32 s56, s55, 12
	s_and_b32 s56, s56, 15
	s_lshl_b32 s56, s56, 15
	s_add_i32 s42, s56, 0xfff68000
	s_add_i32 s56, s55, 13
	s_and_b32 s56, s56, 15
	s_lshl_b32 s56, s56, 15
	s_add_i32 s43, s56, 0xfff68000
	s_add_i32 s56, s55, 14
	s_and_b32 s56, s56, 15
	s_lshl_b32 s56, s56, 15
	s_add_i32 s44, s56, 0xfff68000
	s_add_i32 s56, s55, 15
	s_and_b32 s56, s56, 15
	s_lshl_b32 s56, s56, 15
	s_add_i32 s45, s56, 0xfff68000
	s_add_i32 s56, s55, 16
	s_and_b32 s56, s56, 15
	s_lshl_b32 s56, s56, 15
	s_add_i32 s46, s56, 0xfffe8000
	s_add_i32 s56, s55, 17
	s_and_b32 s56, s56, 15
	s_lshl_b32 s56, s56, 15
	s_add_i32 s47, s56, 0xfffe8000
	s_add_i32 s56, s55, 18
	s_and_b32 s56, s56, 15
	s_lshl_b32 s56, s56, 15
	s_add_i32 s48, s56, 0xfffe8000
	s_add_i32 s56, s55, 19
	s_and_b32 s56, s56, 15
	s_lshl_b32 s56, s56, 15
	s_add_i32 s49, s56, 0xfffe8000
	s_add_i32 s56, s55, 0
	s_and_b32 s56, s56, 15
	s_lshr_b32 s56, s56, 2
	s_add_i32 s57, s55, 12
	s_and_b32 s57, s57, 15
	s_lshr_b32 s57, s57, 2
	s_sub_i32 s56, s56, s57
	s_lshl_b32 s64, s56, 8
	s_add_i32 s56, s55, 1
	s_and_b32 s56, s56, 15
	s_lshr_b32 s56, s56, 2
	s_add_i32 s57, s55, 13
	s_and_b32 s57, s57, 15
	s_lshr_b32 s57, s57, 2
	s_sub_i32 s56, s56, s57
	s_lshl_b32 s65, s56, 8
	s_add_i32 s56, s55, 2
	s_and_b32 s56, s56, 15
	s_lshr_b32 s56, s56, 2
	s_add_i32 s57, s55, 14
	s_and_b32 s57, s57, 15
	s_lshr_b32 s57, s57, 2
	s_sub_i32 s56, s56, s57
	s_lshl_b32 s66, s56, 8
	s_add_i32 s56, s55, 3
	s_and_b32 s56, s56, 15
	s_lshr_b32 s56, s56, 2
	s_add_i32 s57, s55, 15
	s_and_b32 s57, s57, 15
	s_lshr_b32 s57, s57, 2
	s_sub_i32 s56, s56, s57
	s_lshl_b32 s67, s56, 8
	s_add_i32 s56, s55, 4
	s_and_b32 s56, s56, 15
	s_lshr_b32 s56, s56, 2
	s_add_i32 s57, s55, 16
	s_and_b32 s57, s57, 15
	s_lshr_b32 s57, s57, 2
	s_sub_i32 s56, s56, s57
	s_lshl_b32 s68, s56, 8
	s_add_i32 s56, s55, 5
	s_and_b32 s56, s56, 15
	s_lshr_b32 s56, s56, 2
	s_add_i32 s57, s55, 17
	s_and_b32 s57, s57, 15
	s_lshr_b32 s57, s57, 2
	s_sub_i32 s56, s56, s57
	s_lshl_b32 s69, s56, 8
	s_add_i32 s56, s55, 6
	s_and_b32 s56, s56, 15
	s_lshr_b32 s56, s56, 2
	s_add_i32 s57, s55, 18
	s_and_b32 s57, s57, 15
	s_lshr_b32 s57, s57, 2
	s_sub_i32 s56, s56, s57
	s_lshl_b32 s70, s56, 8
	s_add_i32 s56, s55, 7
	s_and_b32 s56, s56, 15
	s_lshr_b32 s56, s56, 2
	s_add_i32 s57, s55, 19
	s_and_b32 s57, s57, 15
	s_lshr_b32 s57, s57, 2
	s_sub_i32 s56, s56, s57
	s_lshl_b32 s71, s56, 8
	s_add_i32 s56, s55, 8
	s_and_b32 s56, s56, 15
	s_lshr_b32 s56, s56, 2
	s_add_i32 s57, s55, 20
	s_and_b32 s57, s57, 15
	s_lshr_b32 s57, s57, 2
	s_sub_i32 s56, s56, s57
	s_lshl_b32 s72, s56, 8
	s_add_i32 s56, s55, 9
	s_and_b32 s56, s56, 15
	s_lshr_b32 s56, s56, 2
	s_add_i32 s57, s55, 21
	s_and_b32 s57, s57, 15
	s_lshr_b32 s57, s57, 2
	s_sub_i32 s56, s56, s57
	s_lshl_b32 s73, s56, 8
	s_add_i32 s56, s55, 10
	s_and_b32 s56, s56, 15
	s_lshr_b32 s56, s56, 2
	s_add_i32 s57, s55, 22
	s_and_b32 s57, s57, 15
	s_lshr_b32 s57, s57, 2
	s_sub_i32 s56, s56, s57
	s_lshl_b32 s74, s56, 8
	s_add_i32 s56, s55, 11
	s_and_b32 s56, s56, 15
	s_lshr_b32 s56, s56, 2
	s_add_i32 s57, s55, 23
	s_and_b32 s57, s57, 15
	s_lshr_b32 s57, s57, 2
	s_sub_i32 s56, s56, s57
	s_lshl_b32 s75, s56, 8
	s_add_i32 s56, s55, 12
	s_and_b32 s56, s56, 15
	s_lshr_b32 s56, s56, 2
	s_add_i32 s57, s55, 24
	s_and_b32 s57, s57, 15
	s_lshr_b32 s57, s57, 2
	s_sub_i32 s56, s56, s57
	s_lshl_b32 s76, s56, 8
	s_add_i32 s56, s55, 13
	s_and_b32 s56, s56, 15
	s_lshr_b32 s56, s56, 2
	s_add_i32 s57, s55, 25
	s_and_b32 s57, s57, 15
	s_lshr_b32 s57, s57, 2
	s_sub_i32 s56, s56, s57
	s_lshl_b32 s77, s56, 8
	s_add_i32 s56, s55, 14
	s_and_b32 s56, s56, 15
	s_lshr_b32 s56, s56, 2
	s_add_i32 s57, s55, 26
	s_and_b32 s57, s57, 15
	s_lshr_b32 s57, s57, 2
	s_sub_i32 s56, s56, s57
	s_lshl_b32 s78, s56, 8
	s_add_i32 s56, s55, 15
	s_and_b32 s56, s56, 15
	s_lshr_b32 s56, s56, 2
	s_add_i32 s57, s55, 27
	s_and_b32 s57, s57, 15
	s_lshr_b32 s57, s57, 2
	s_sub_i32 s56, s56, s57
	s_lshl_b32 s79, s56, 8
	s_add_i32 s56, s55, 12
	s_and_b32 s56, s56, 15
	s_lshr_b32 s56, s56, 2
	s_lshl_b32 s80, s56, 8
	s_add_i32 s56, s55, 13
	s_and_b32 s56, s56, 15
	s_lshr_b32 s56, s56, 2
	s_lshl_b32 s81, s56, 8
	s_add_i32 s56, s55, 14
	s_and_b32 s56, s56, 15
	s_lshr_b32 s56, s56, 2
	s_lshl_b32 s82, s56, 8
	s_add_i32 s56, s55, 15
	s_and_b32 s56, s56, 15
	s_lshr_b32 s56, s56, 2
	s_lshl_b32 s83, s56, 8
	s_and_b32 s56, s20, 1
	s_cmp_eq_u32 s56, 1
	s_cselect_b64 s[84:85], -1, 0
	buffer_load_dwordx4 v[58:61], v147, s[16:19], s60 offen
	buffer_load_dwordx4 v[54:57], v147, s[16:19], s60 offen offset:1024
	buffer_load_dwordx4 v[50:53], v147, s[16:19], s60 offen offset:2048
	buffer_load_dwordx4 v[38:41], v147, s[16:19], s60 offen offset:3072
	s_mov_b32 s10, 0xffff
	s_mov_b32 s0, 0x8000
	buffer_load_dwordx4 v[94:97], v147, s[16:19], s61 offen
	buffer_load_dwordx4 v[90:93], v147, s[16:19], s61 offen offset:1024
	buffer_load_dwordx4 v[78:81], v147, s[16:19], s61 offen offset:2048
	buffer_load_dwordx4 v[34:37], v147, s[16:19], s61 offen offset:3072
	s_mov_b32 s0, 0x10000
	buffer_load_dwordx4 v[82:85], v147, s[16:19], s62 offen
	buffer_load_dwordx4 v[70:73], v147, s[16:19], s62 offen offset:1024
	buffer_load_dwordx4 v[62:65], v147, s[16:19], s62 offen offset:2048
	buffer_load_dwordx4 v[42:45], v147, s[16:19], s62 offen offset:3072
	s_mov_b32 s0, 0x18000
	buffer_load_dwordx4 v[86:89], v147, s[16:19], s63 offen
	buffer_load_dwordx4 v[74:77], v147, s[16:19], s63 offen offset:1024
	buffer_load_dwordx4 v[66:69], v147, s[16:19], s63 offen offset:2048
	buffer_load_dwordx4 v[46:49], v147, s[16:19], s63 offen offset:3072
	s_waitcnt vmcnt(44)
	v_cvt_f16_f32_e32 v173, v174
	s_waitcnt vmcnt(43)
	v_cvt_f16_f32_e32 v175, v175
	v_lshlrev_b32_e32 v174, 1, v0
	v_or_b32_e32 v176, 0x12400, v174
	ds_write_b16 v176, v173
	v_or_b32_e32 v173, 0x12800, v174
	ds_write_b16 v173, v175
	v_add_u32_e32 v173, 0x12c00, v172
	s_mov_b32 s11, 1
	s_waitcnt vmcnt(39)
	ds_write_b128 v173, v[160:163]
	ds_write_b128 v173, v[148:151] offset:8192
	ds_write_b128 v173, v[152:155] offset:16384
	ds_write_b128 v173, v[156:159] offset:24576
	v_add_u32_e32 v148, 0x1ac00, v172
	s_cmpk_lt_u32 s22, 0x100
	s_waitcnt vmcnt(38)
	ds_write_b128 v148, v[164:167]
	s_waitcnt vmcnt(37)
	ds_write_b128 v148, v[168:171] offset:8192
	s_cbranch_scc1 .LBB1_2
	s_setprio 3
.LBB1_2:
	v_lshrrev_b32_e32 v151, 4, v137
	s_lshl_b64 s[6:7], s[2:3], 4
	v_cmp_eq_u32_e64 s[2:3], 1, v151
	s_waitcnt vmcnt(31)
	v_cvt_f16_f32_e32 v8, v8
	v_cmp_gt_u32_e32 vcc, 16, v137
	s_waitcnt vmcnt(29)
	v_cndmask_b32_e64 v116, 0, v116, s[2:3]
	s_waitcnt vmcnt(21)
	v_cndmask_b32_e64 v100, 0, v100, s[2:3]
	v_cmp_eq_u32_e64 s[0:1], 2, v151
	v_cndmask_b32_e64 v114, 0, v114, s[2:3]
	v_cndmask_b32_e64 v115, 0, v115, s[2:3]
	v_cndmask_b32_e32 v6, v116, v6, vcc
	v_cndmask_b32_e64 v116, 0, v117, s[2:3]
	v_cndmask_b32_e64 v108, 0, v108, s[2:3]
	v_cndmask_b32_e32 v26, v100, v26, vcc
	v_cvt_f16_f32_e32 v29, v29
	v_cndmask_b32_e64 v100, 0, v101, s[2:3]
	v_cndmask_b32_e32 v28, 0, v28, vcc
	v_cndmask_b32_e64 v152, 0, 1.0, s[0:1]
	v_cndmask_b32_e32 v114, v114, v120, vcc
	v_cndmask_b32_e32 v115, v115, v121, vcc
	v_cndmask_b32_e32 v7, v116, v7, vcc
	v_cndmask_b32_e64 v106, 0, v106, s[2:3]
	v_cndmask_b32_e64 v107, 0, v107, s[2:3]
	v_cndmask_b32_e32 v14, v108, v14, vcc
	v_cndmask_b32_e64 v108, 0, v109, s[2:3]
	v_cndmask_b32_e32 v27, v100, v27, vcc
	v_cvt_f16_f32_e32 v100, v28
	v_cndmask_b32_e32 v116, 0, v8, vcc
	v_cvt_pk_f16_f32 v8, v6, v7
	v_cvt_pk_f16_f32 v7, v114, v115
	v_cndmask_b32_e64 v114, v152, v140, s[2:3]
	v_cndmask_b32_e32 v106, v106, v112, vcc
	v_cndmask_b32_e32 v107, v107, v113, vcc
	v_cndmask_b32_e32 v15, v108, v15, vcc
	v_cndmask_b32_e64 v98, 0, v98, s[2:3]
	v_cndmask_b32_e64 v99, 0, v99, s[2:3]
	v_cndmask_b32_e32 v110, v114, v110, vcc
	v_cndmask_b32_e64 v114, 0, v141, s[2:3]
	v_cndmask_b32_e32 v108, 0, v16, vcc
	v_cvt_pk_f16_f32 v16, v14, v15
	v_cvt_pk_f16_f32 v15, v106, v107
	v_cndmask_b32_e64 v106, v152, v138, s[2:3]
	v_cndmask_b32_e32 v98, v98, v104, vcc
	v_cndmask_b32_e32 v99, v99, v105, vcc
	v_cndmask_b32_e32 v111, v114, v111, vcc
	v_cndmask_b32_e32 v102, v106, v102, vcc
	v_cndmask_b32_e64 v106, 0, v139, s[2:3]
	v_cndmask_b32_e32 v29, 0, v29, vcc
	v_cvt_pk_f16_f32 v28, v26, v27
	v_cvt_pk_f16_f32 v27, v98, v99
	v_lshlrev_b32_e32 v101, 10, v1
	v_bitop3_b32 v98, v151, v0, 3 bitop3:0x78
	v_lshl_add_u64 v[130:131], s[4:5], 0, v[130:131]
	v_cvt_f16_f32_e32 v4, v4
	v_cvt_pk_f16_f32 v14, v110, v111
	v_cndmask_b32_e32 v103, v106, v103, vcc
	v_pack_b32_f16 v29, v100, v29
	v_lshl_or_b32 v111, v98, 4, v101
	v_lshlrev_b32_e32 v100, 4, v1
	s_movk_i32 s4, 0xc0
	v_cndmask_b32_e64 v124, 0, v124, s[2:3]
	v_cvt_pk_f16_f32 v26, v102, v103
	v_and_b32_e32 v112, 0xc0, v100
	v_bitop3_b32 v100, v100, s4, v111 bitop3:0x26
	s_lshl_b32 s4, s20, 3
	v_lshrrev_b32_e32 v102, 5, v137
	v_lshrrev_b32_e32 v104, 1, v137
	v_cndmask_b32_e64 v122, 0, v122, s[2:3]
	v_cndmask_b32_e64 v123, 0, v123, s[2:3]
	v_cndmask_b32_e32 v2, v124, v2, vcc
	v_cvt_f16_f32_e32 v5, v5
	v_cndmask_b32_e64 v124, 0, v125, s[2:3]
	v_cvt_f16_f32_e32 v9, v9
	v_or_b32_e32 v103, s4, v102
	v_and_or_b32 v110, v104, 8, v101
	v_bitop3_b32 v101, s4, v1, v102 bitop3:0x36
	s_lshl_b32 s4, s20, 4
	v_cndmask_b32_e32 v122, v122, v128, vcc
	v_cndmask_b32_e32 v123, v123, v129, vcc
	v_cndmask_b32_e32 v3, v124, v3, vcc
	v_cndmask_b32_e32 v17, 0, v17, vcc
	v_lshlrev_b32_e32 v107, 4, v101
	v_bitop3_b32 v101, v103, v1, 2 bitop3:0x36
	s_add_i32 s4, s4, 0x10000
	v_bfe_u32 v0, v0, 4, 2
	v_cndmask_b32_e64 v144, v152, v144, s[2:3]
	v_cndmask_b32_e32 v124, 0, v4, vcc
	v_cvt_pk_f16_f32 v4, v2, v3
	v_cvt_pk_f16_f32 v3, v122, v123
	v_cndmask_b32_e64 v122, v152, v142, s[2:3]
	v_cvt_pk_f16_f32 v17, v108, v17
	s_movk_i32 s5, 0x80
	v_lshlrev_b32_e32 v108, 4, v101
	v_bitop3_b32 v101, v103, v1, 4 bitop3:0x36
	s_cmp_lt_u32 s22, 64
	v_lshlrev_b32_e32 v104, 5, v0
	v_lshlrev_b32_e32 v0, 6, v0
	v_cndmask_b32_e32 v126, v144, v126, vcc
	v_cndmask_b32_e64 v144, 0, v145, s[2:3]
	v_cndmask_b32_e32 v118, v122, v118, vcc
	v_cndmask_b32_e64 v122, 0, v143, s[2:3]
	v_bitop3_b32 v99, v112, s5, v111 bitop3:0x36
	v_lshlrev_b32_e32 v109, 4, v101
	v_bitop3_b32 v101, v103, v1, 6 bitop3:0x36
	v_lshl_or_b32 v105, s20, 8, v0
	v_mov_b32_e32 v0, 0x1ec00
	s_cselect_b64 s[4:5], -1, 0
	v_cndmask_b32_e32 v127, v144, v127, vcc
	v_cndmask_b32_e32 v5, 0, v5, vcc
	v_cndmask_b32_e32 v119, v122, v119, vcc
	v_cndmask_b32_e32 v9, 0, v9, vcc
	v_lshlrev_b32_e32 v113, 4, v101
	v_lshlrev_b32_e32 v101, 5, v1
	v_lshl_add_u32 v106, v137, 6, v0
	s_cmp_eq_u32 s20, 0
	s_cselect_b32 s31, 0, 0xffff1d00
	v_add_u32_e32 v106, s31, v106
	v_cndmask_b32_e64 v0, 0, 1, s[4:5]
	v_lshl_add_u64 v[132:133], s[8:9], 0, v[132:133]
	v_or_b32_e32 v148, 0x400, v147
	v_or_b32_e32 v149, 0x800, v147
	v_or_b32_e32 v150, 0xc00, v147
	v_cvt_pk_f16_f32 v2, v126, v127
	v_pack_b32_f16 v5, v124, v5
	v_cvt_pk_f16_f32 v6, v118, v119
	v_pack_b32_f16 v9, v116, v9
	v_bitop3_b32 v98, v112, 64, v111 bitop3:0x36
	v_lshl_or_b32 v104, s20, 7, v104
	s_mov_b32 s22, 0x98000
	s_mov_b32 s23, 0x5040100
	s_mov_b32 s24, 0x7060302
	v_add_u32_e32 v107, v107, v110
	v_add_u32_e32 v108, v108, v110
	v_add_u32_e32 v109, v109, v110
	v_add_u32_e32 v110, v113, v110
	v_add_u32_e32 v111, v112, v111
	v_lshlrev_b32_e32 v113, 4, v137
	v_or_b32_e32 v113, 0x10000, v113
	s_lshr_b32 s28, s20, 2
	s_and_b32 s29, s20, 3
	s_lshl_b32 s28, s28, 10
	s_lshl_b32 s29, s29, 2
	s_add_i32 s28, s28, s29
	v_add_u32_e32 v112, s28, v113
	v_cmp_eq_u32_e64 s[26:27], 3, v151
	v_add_u32_e32 v114, 0x12400, v101
	v_and_b32_e32 v109, 3, v137
	v_cmp_eq_u32_e64 s[86:87], 0, v109
	v_mov_b32_e32 v110, 0xffff6e00
	v_mov_b32_e32 v109, 0x400
	v_cndmask_b32_e64 v104, v110, v104, s[86:87]
	v_cndmask_b32_e64 v109, 0, v109, s[86:87]
	v_mov_b32_e32 v110, 0x11a00
	ds_write2_b32 v110, v136, v136 offset1:1
	ds_write2_b32 v110, v136, v136 offset0:2 offset1:3
	ds_write2_b32 v110, v136, v136 offset0:4 offset1:5
	ds_write2_b32 v110, v136, v136 offset0:6 offset1:7
	v_mov_b32_e32 v121, v111
	v_mov_b32_e32 v144, v98
	v_cndmask_b32_e64 v111, v111, v99, s[84:85]
	v_cndmask_b32_e64 v99, v99, v121, s[84:85]
	v_cndmask_b32_e64 v98, v98, v100, s[84:85]
	v_cndmask_b32_e64 v100, v100, v144, s[84:85]
	v_add_u32_e32 v111, s80, v111
	v_add_u32_e32 v98, s81, v98
	v_add_u32_e32 v99, s82, v99
	v_add_u32_e32 v100, s83, v100
	v_and_b32_e32 v108, 15, v137
	s_lshl_b32 s31, s20, 3
	v_add_u32_e32 v107, s31, v151
	v_xor_b32_e32 v107, v107, v108
	v_lshlrev_b32_e32 v107, 4, v107
	v_lshl_or_b32 v107, v108, 10, v107
	v_xor_b32_e32 v108, 64, v107
	v_cmp_ne_u32_e64 s[4:5], 1, v0
	s_waitcnt vmcnt(16)
	v_cndmask_b32_e64 v1, v30, v134, s[0:1]
	v_bfi_b32 v30, s10, v1, v30
	v_perm_b32 v1, v22, v134, s24
	v_cndmask_b32_e64 v22, v22, v1, s[0:1]
	v_bfi_b32 v1, s10, v135, v18
	v_perm_b32 v121, v10, v135, s24
	v_cndmask_b32_e64 v18, v18, v1, s[0:1]
	v_cndmask_b32_e64 v10, v10, v121, s[0:1]
	v_mov_b32_e32 v121, v136
	v_mov_b32_e32 v144, v136
	v_mov_b32_e32 v145, v136
	v_mov_b32_e32 v0, v136
	v_mov_b32_e32 v1, v136
	s_waitcnt lgkmcnt(0)
	s_barrier
	ds_read_u16 v102, v114
	ds_read_u16 v103, v114 offset:512
	ds_read_u16 v115, v114 offset:1024
	ds_read_u16 v116, v114 offset:1536
	v_add_u32_e32 v0, 0x12c00, v105
	ds_read_b128 v[240:243], v0
	ds_read_b128 v[244:247], v0 offset:16
	ds_read_b128 v[248:251], v0 offset:32
	ds_read_b128 v[252:255], v0 offset:48
	v_add_u32_e32 v114, 2, v114
	s_waitcnt lgkmcnt(0)
	s_branch .LBB1_4
.LBB1_4:
	s_and_saveexec_b64 s[8:9], s[2:3]
	v_perm_b32 v5, v1, v102, s23
	v_perm_b32 v9, v121, v103, s23
	v_perm_b32 v17, v144, v115, s23
	v_perm_b32 v29, v145, v116, s23
	s_or_b64 exec, exec, s[8:9]
	v_mfma_f32_16x16x32_f16 v[164:167], v[30:33], v[2:5], 0
	v_mfma_f32_16x16x32_f16 v[180:183], v[22:25], v[2:5], 0
	s_cmp_lg_u32 s22, 0x818000
	v_mfma_f32_16x16x32_f16 v[168:171], v[30:33], v[6:9], 0
	v_mfma_f32_16x16x32_f16 v[184:187], v[22:25], v[6:9], 0
	s_cselect_b32 s9, s11, 15
	v_mfma_f32_16x16x32_f16 v[172:175], v[30:33], v[14:17], 0
	v_mfma_f32_16x16x32_f16 v[188:191], v[22:25], v[14:17], 0
	v_mfma_f32_16x16x32_f16 v[176:179], v[30:33], v[26:29], 0
	v_mfma_f32_16x16x32_f16 v[192:195], v[22:25], v[26:29], 0
	v_mfma_f32_16x16x32_f16 v[196:199], v[18:21], v[2:5], 0
	v_cvt_pk_f16_f32 v122, v164, v165
	v_cvt_pk_f16_f32 v123, v166, v167
	v_pk_max_f16 v122, v122, 0
	v_pk_max_f16 v123, v123, 0
	v_cvt_pk_f16_f32 v124, v180, v181
	v_cvt_pk_f16_f32 v125, v182, v183
	v_pk_max_f16 v124, v124, 0
	v_pk_max_f16 v125, v125, 0
	ds_write_b128 v107, v[122:125]
	v_mfma_f32_16x16x32_f16 v[212:215], v[10:13], v[2:5], 0
	v_cvt_pk_f16_f32 v126, v168, v169
	v_cvt_pk_f16_f32 v127, v170, v171
	v_pk_max_f16 v126, v126, 0
	v_pk_max_f16 v127, v127, 0
	v_cvt_pk_f16_f32 v128, v184, v185
	v_cvt_pk_f16_f32 v129, v186, v187
	v_pk_max_f16 v128, v128, 0
	v_pk_max_f16 v129, v129, 0
	ds_write_b128 v107, v[126:129] offset:16384
	v_mfma_f32_16x16x32_f16 v[200:203], v[18:21], v[6:9], 0
	v_cvt_pk_f16_f32 v134, v172, v173
	v_cvt_pk_f16_f32 v135, v174, v175
	v_pk_max_f16 v134, v134, 0
	v_pk_max_f16 v135, v135, 0
	v_cvt_pk_f16_f32 v136, v188, v189
	v_cvt_pk_f16_f32 v137, v190, v191
	v_pk_max_f16 v136, v136, 0
	v_pk_max_f16 v137, v137, 0
	ds_write_b128 v107, v[134:137] offset:32768
	v_mfma_f32_16x16x32_f16 v[216:219], v[10:13], v[6:9], 0
	v_cvt_pk_f16_f32 v138, v176, v177
	v_cvt_pk_f16_f32 v139, v178, v179
	v_pk_max_f16 v138, v138, 0
	v_pk_max_f16 v139, v139, 0
	v_cvt_pk_f16_f32 v140, v192, v193
	v_cvt_pk_f16_f32 v141, v194, v195
	v_pk_max_f16 v140, v140, 0
	v_pk_max_f16 v141, v141, 0
	ds_write_b128 v107, v[138:141] offset:49152
	v_mfma_f32_16x16x32_f16 v[204:207], v[18:21], v[14:17], 0
	v_cvt_pk_f16_f32 v142, v196, v197
	v_cvt_pk_f16_f32 v143, v198, v199
	v_pk_max_f16 v142, v142, 0
	v_pk_max_f16 v143, v143, 0
	v_cvt_pk_f16_f32 v144, v212, v213
	v_cvt_pk_f16_f32 v145, v214, v215
	v_pk_max_f16 v144, v144, 0
	v_pk_max_f16 v145, v145, 0
	ds_write_b128 v108, v[142:145]
	v_mfma_f32_16x16x32_f16 v[220:223], v[10:13], v[14:17], 0
	v_cvt_pk_f16_f32 v152, v200, v201
	v_cvt_pk_f16_f32 v153, v202, v203
	v_pk_max_f16 v152, v152, 0
	v_pk_max_f16 v153, v153, 0
	v_cvt_pk_f16_f32 v154, v216, v217
	v_cvt_pk_f16_f32 v155, v218, v219
	v_pk_max_f16 v154, v154, 0
	v_pk_max_f16 v155, v155, 0
	ds_write_b128 v108, v[152:155] offset:16384
	v_mfma_f32_16x16x32_f16 v[208:211], v[18:21], v[26:29], 0
	v_mfma_f32_16x16x32_f16 v[224:227], v[10:13], v[26:29], 0
	v_cvt_pk_f16_f32 v156, v204, v205
	v_cvt_pk_f16_f32 v157, v206, v207
	v_pk_max_f16 v156, v156, 0
	v_pk_max_f16 v157, v157, 0
	v_cvt_pk_f16_f32 v158, v220, v221
	v_cvt_pk_f16_f32 v159, v222, v223
	v_pk_max_f16 v158, v158, 0
	v_pk_max_f16 v159, v159, 0
	ds_write_b128 v108, v[156:159] offset:32768
	v_cvt_pk_f16_f32 v160, v208, v209
	v_cvt_pk_f16_f32 v161, v210, v211
	v_pk_max_f16 v160, v160, 0
	v_pk_max_f16 v161, v161, 0
	v_cvt_pk_f16_f32 v162, v224, v225
	v_cvt_pk_f16_f32 v163, v226, v227
	v_pk_max_f16 v162, v162, 0
	v_pk_max_f16 v163, v163, 0
	ds_write_b128 v108, v[160:163] offset:49152
	v_add_u32_e32 v111, s64, v111
	v_add_u32_e32 v98, s65, v98
	s_lshl_b32 s20, s9, 7
	v_lshl_add_u64 v[0:1], s[20:21], 3, v[132:133]
	s_add_i32 s25, s22, s34
	s_lshl_b32 s8, s9, 8
	buffer_load_dwordx4 v[192:195], v147, s[16:19], s25 offen
	buffer_load_dwordx4 v[196:199], v148, s[16:19], s25 offen
	buffer_load_dwordx4 v[200:203], v149, s[16:19], s25 offen
	buffer_load_dwordx4 v[204:207], v150, s[16:19], s25 offen
	s_waitcnt vmcnt(19)
	v_mfma_f32_16x16x32_f16 v[164:167], v[58:61], v[122:125], v[240:243]
	v_mfma_f32_16x16x32_f16 v[168:171], v[58:61], v[126:129], v[240:243]
	v_mfma_f32_16x16x32_f16 v[172:175], v[58:61], v[134:137], v[240:243]
	v_mfma_f32_16x16x32_f16 v[10:13], v[58:61], v[138:141], v[240:243]
	s_waitcnt vmcnt(18)
	v_mfma_f32_16x16x32_f16 v[58:61], v[54:57], v[122:125], v[244:247]
	v_mfma_f32_16x16x32_f16 v[176:179], v[54:57], v[126:129], v[244:247]
	v_mfma_f32_16x16x32_f16 v[180:183], v[54:57], v[134:137], v[244:247]
	v_mfma_f32_16x16x32_f16 v[18:21], v[54:57], v[138:141], v[244:247]
	s_waitcnt vmcnt(17)
	v_mfma_f32_16x16x32_f16 v[54:57], v[50:53], v[122:125], v[248:251]
	v_mfma_f32_16x16x32_f16 v[184:187], v[50:53], v[126:129], v[248:251]
	v_mfma_f32_16x16x32_f16 v[188:191], v[50:53], v[134:137], v[248:251]
	v_mfma_f32_16x16x32_f16 v[22:25], v[50:53], v[138:141], v[248:251]
	s_waitcnt vmcnt(16)
	v_mfma_f32_16x16x32_f16 v[50:53], v[38:41], v[122:125], v[252:255]
	v_mfma_f32_16x16x32_f16 v[122:125], v[38:41], v[126:129], v[252:255]
	v_mfma_f32_16x16x32_f16 v[126:129], v[38:41], v[134:137], v[252:255]
	v_mfma_f32_16x16x32_f16 v[38:41], v[38:41], v[138:141], v[252:255]
	s_add_i32 s9, s22, s35
	s_waitcnt vmcnt(15)
	v_mfma_f32_16x16x32_f16 v[164:167], v[94:97], v[142:145], v[164:167]
	v_mfma_f32_16x16x32_f16 v[168:171], v[94:97], v[152:155], v[168:171]
	s_waitcnt vmcnt(14)
	v_mfma_f32_16x16x32_f16 v[58:61], v[90:93], v[142:145], v[58:61]
	v_mfma_f32_16x16x32_f16 v[176:179], v[90:93], v[152:155], v[176:179]
	s_waitcnt vmcnt(13)
	v_mfma_f32_16x16x32_f16 v[54:57], v[78:81], v[142:145], v[54:57]
	v_mfma_f32_16x16x32_f16 v[184:187], v[78:81], v[152:155], v[184:187]
	s_waitcnt vmcnt(12)
	v_mfma_f32_16x16x32_f16 v[50:53], v[34:37], v[142:145], v[50:53]
	buffer_load_dwordx4 v[140:143], v147, s[16:19], s9 offen
	buffer_load_dwordx4 v[220:223], v148, s[16:19], s9 offen
	v_mfma_f32_16x16x32_f16 v[122:125], v[34:37], v[152:155], v[122:125]
	buffer_load_dwordx4 v[152:155], v149, s[16:19], s9 offen
	buffer_load_dwordx4 v[224:227], v150, s[16:19], s9 offen
	s_mov_b32 s9, s21
	s_waitcnt lgkmcnt(0)
	s_barrier
	v_add_u32_e32 v99, s66, v99
	ds_read_b128 v[136:139], v99
	ds_read_b128 v[208:211], v99 offset:16384
	ds_read_b128 v[212:215], v99 offset:32768
	ds_read_b128 v[216:219], v99 offset:49152
	v_mfma_f32_16x16x32_f16 v[172:175], v[94:97], v[156:159], v[172:175]
	v_mfma_f32_16x16x32_f16 v[94:97], v[94:97], v[160:163], v[10:13]
	s_nop 2
	v_lshl_add_u64 v[10:11], s[8:9], 4, v[130:131]
	v_mfma_f32_16x16x32_f16 v[180:183], v[90:93], v[156:159], v[180:183]
	v_mfma_f32_16x16x32_f16 v[90:93], v[90:93], v[160:163], v[18:21]
	v_mfma_f32_16x16x32_f16 v[188:191], v[78:81], v[156:159], v[188:191]
	v_mfma_f32_16x16x32_f16 v[78:81], v[78:81], v[160:163], v[22:25]
	global_load_dwordx4 v[30:33], v[10:11], off
	s_nop 1
	global_load_dwordx4 v[22:25], v[10:11], off offset:1024
	global_load_dwordx4 v[18:21], v[10:11], off offset:2048
	s_nop 0
	global_load_dwordx4 v[10:13], v[10:11], off offset:3072
	s_nop 0
	global_load_dwordx2 v[134:135], v[0:1], off
	v_mfma_f32_16x16x32_f16 v[126:129], v[34:37], v[156:159], v[126:129]
	v_mfma_f32_16x16x32_f16 v[34:37], v[34:37], v[160:163], v[38:41]
	s_nop 2
	v_add_u32_e32 v100, s67, v100
	ds_read_b128 v[38:41], v100
	ds_read_b128 v[156:159], v100 offset:16384
	ds_read_b128 v[160:163], v100 offset:32768
	ds_read_b128 v[228:231], v100 offset:49152
	s_add_i32 s8, s22, s36
	s_waitcnt vmcnt(20) lgkmcnt(7)
	v_mfma_f32_16x16x32_f16 v[164:167], v[82:85], v[136:139], v[164:167]
	s_waitcnt lgkmcnt(6)
	v_mfma_f32_16x16x32_f16 v[168:171], v[82:85], v[208:211], v[168:171]
	s_waitcnt lgkmcnt(5)
	v_mfma_f32_16x16x32_f16 v[172:175], v[82:85], v[212:215], v[172:175]
	s_waitcnt lgkmcnt(4)
	v_mfma_f32_16x16x32_f16 v[82:85], v[82:85], v[216:219], v[94:97]
	s_waitcnt vmcnt(19)
	v_mfma_f32_16x16x32_f16 v[58:61], v[70:73], v[136:139], v[58:61]
	v_mfma_f32_16x16x32_f16 v[94:97], v[70:73], v[208:211], v[176:179]
	v_mfma_f32_16x16x32_f16 v[176:179], v[70:73], v[212:215], v[180:183]
	v_mfma_f32_16x16x32_f16 v[70:73], v[70:73], v[216:219], v[90:93]
	s_waitcnt vmcnt(18)
	v_mfma_f32_16x16x32_f16 v[54:57], v[62:65], v[136:139], v[54:57]
	v_mfma_f32_16x16x32_f16 v[90:93], v[62:65], v[208:211], v[184:187]
	v_mfma_f32_16x16x32_f16 v[180:183], v[62:65], v[212:215], v[188:191]
	v_mfma_f32_16x16x32_f16 v[62:65], v[62:65], v[216:219], v[78:81]
	s_waitcnt vmcnt(17)
	v_mfma_f32_16x16x32_f16 v[50:53], v[42:45], v[136:139], v[50:53]
	v_mfma_f32_16x16x32_f16 v[78:81], v[42:45], v[208:211], v[122:125]
	v_mfma_f32_16x16x32_f16 v[122:125], v[42:45], v[212:215], v[126:129]
	s_nop 2
	buffer_load_dwordx4 v[126:129], v147, s[16:19], s8 offen
	buffer_load_dwordx4 v[136:139], v148, s[16:19], s8 offen
	buffer_load_dwordx4 v[184:187], v149, s[16:19], s8 offen
	buffer_load_dwordx4 v[188:191], v150, s[16:19], s8 offen
	v_mfma_f32_16x16x32_f16 v[34:37], v[42:45], v[216:219], v[34:37]
	v_add_u32_e32 v111, s68, v111
	ds_read_b128 v[42:45], v111
	ds_read_b128 v[208:211], v111 offset:16384
	ds_read_b128 v[212:215], v111 offset:32768
	ds_read_b128 v[216:219], v111 offset:49152
	s_add_i32 s8, s22, s37
	s_waitcnt vmcnt(20) lgkmcnt(7)
	v_mfma_f32_16x16x32_f16 v[164:167], v[86:89], v[38:41], v[164:167]
	s_waitcnt lgkmcnt(6)
	v_mfma_f32_16x16x32_f16 v[168:171], v[86:89], v[156:159], v[168:171]
	s_waitcnt lgkmcnt(5)
	v_mfma_f32_16x16x32_f16 v[172:175], v[86:89], v[160:163], v[172:175]
	s_waitcnt lgkmcnt(4)
	v_mfma_f32_16x16x32_f16 v[82:85], v[86:89], v[228:231], v[82:85]
	s_waitcnt vmcnt(19)
	v_mfma_f32_16x16x32_f16 v[58:61], v[74:77], v[38:41], v[58:61]
	v_mfma_f32_16x16x32_f16 v[86:89], v[74:77], v[156:159], v[94:97]
	v_mfma_f32_16x16x32_f16 v[94:97], v[74:77], v[160:163], v[176:179]
	v_mfma_f32_16x16x32_f16 v[70:73], v[74:77], v[228:231], v[70:73]
	s_waitcnt vmcnt(18)
	v_mfma_f32_16x16x32_f16 v[54:57], v[66:69], v[38:41], v[54:57]
	v_mfma_f32_16x16x32_f16 v[74:77], v[66:69], v[156:159], v[90:93]
	v_mfma_f32_16x16x32_f16 v[90:93], v[66:69], v[160:163], v[180:183]
	v_mfma_f32_16x16x32_f16 v[62:65], v[66:69], v[228:231], v[62:65]
	s_waitcnt vmcnt(17)
	v_mfma_f32_16x16x32_f16 v[38:41], v[46:49], v[38:41], v[50:53]
	v_mfma_f32_16x16x32_f16 v[50:53], v[46:49], v[156:159], v[78:81]
	v_mfma_f32_16x16x32_f16 v[66:69], v[46:49], v[160:163], v[122:125]
	s_nop 1
	buffer_load_dwordx4 v[78:81], v147, s[16:19], s8 offen
	buffer_load_dwordx4 v[122:125], v148, s[16:19], s8 offen
	buffer_load_dwordx4 v[156:159], v149, s[16:19], s8 offen
	buffer_load_dwordx4 v[160:163], v150, s[16:19], s8 offen
	v_mfma_f32_16x16x32_f16 v[34:37], v[46:49], v[228:231], v[34:37]
	v_add_u32_e32 v98, s69, v98
	ds_read_b128 v[46:49], v98
	ds_read_b128 v[176:179], v98 offset:16384
	ds_read_b128 v[180:183], v98 offset:32768
	ds_read_b128 v[228:231], v98 offset:49152
	s_add_i32 s8, s22, s38
	s_waitcnt vmcnt(20) lgkmcnt(7)
	v_mfma_f32_16x16x32_f16 v[164:167], v[192:195], v[42:45], v[164:167]
	s_waitcnt lgkmcnt(6)
	v_mfma_f32_16x16x32_f16 v[168:171], v[192:195], v[208:211], v[168:171]
	s_waitcnt lgkmcnt(5)
	v_mfma_f32_16x16x32_f16 v[172:175], v[192:195], v[212:215], v[172:175]
	s_waitcnt lgkmcnt(4)
	v_mfma_f32_16x16x32_f16 v[82:85], v[192:195], v[216:219], v[82:85]
	s_waitcnt vmcnt(19)
	v_mfma_f32_16x16x32_f16 v[58:61], v[196:199], v[42:45], v[58:61]
	v_mfma_f32_16x16x32_f16 v[86:89], v[196:199], v[208:211], v[86:89]
	v_mfma_f32_16x16x32_f16 v[94:97], v[196:199], v[212:215], v[94:97]
	v_mfma_f32_16x16x32_f16 v[70:73], v[196:199], v[216:219], v[70:73]
	s_waitcnt vmcnt(18)
	v_mfma_f32_16x16x32_f16 v[54:57], v[200:203], v[42:45], v[54:57]
	v_mfma_f32_16x16x32_f16 v[74:77], v[200:203], v[208:211], v[74:77]
	v_mfma_f32_16x16x32_f16 v[90:93], v[200:203], v[212:215], v[90:93]
	v_mfma_f32_16x16x32_f16 v[62:65], v[200:203], v[216:219], v[62:65]
	s_waitcnt vmcnt(17)
	v_mfma_f32_16x16x32_f16 v[38:41], v[204:207], v[42:45], v[38:41]
	v_mfma_f32_16x16x32_f16 v[42:45], v[204:207], v[208:211], v[50:53]
	v_mfma_f32_16x16x32_f16 v[50:53], v[204:207], v[212:215], v[66:69]
	s_nop 2
	buffer_load_dwordx4 v[66:69], v147, s[16:19], s8 offen
	buffer_load_dwordx4 v[192:195], v148, s[16:19], s8 offen
	buffer_load_dwordx4 v[196:199], v149, s[16:19], s8 offen
	buffer_load_dwordx4 v[200:203], v150, s[16:19], s8 offen
	v_mfma_f32_16x16x32_f16 v[34:37], v[204:207], v[216:219], v[34:37]
	v_add_u32_e32 v99, s70, v99
	ds_read_b128 v[204:207], v99
	ds_read_b128 v[208:211], v99 offset:16384
	ds_read_b128 v[212:215], v99 offset:32768
	ds_read_b128 v[216:219], v99 offset:49152
	s_add_i32 s8, s22, s39
	s_waitcnt vmcnt(20) lgkmcnt(7)
	v_mfma_f32_16x16x32_f16 v[164:167], v[140:143], v[46:49], v[164:167]
	s_waitcnt lgkmcnt(6)
	v_mfma_f32_16x16x32_f16 v[168:171], v[140:143], v[176:179], v[168:171]
	s_waitcnt lgkmcnt(5)
	v_mfma_f32_16x16x32_f16 v[172:175], v[140:143], v[180:183], v[172:175]
	s_waitcnt lgkmcnt(4)
	v_mfma_f32_16x16x32_f16 v[82:85], v[140:143], v[228:231], v[82:85]
	s_waitcnt vmcnt(19)
	v_mfma_f32_16x16x32_f16 v[58:61], v[220:223], v[46:49], v[58:61]
	v_mfma_f32_16x16x32_f16 v[86:89], v[220:223], v[176:179], v[86:89]
	s_waitcnt vmcnt(18)
	v_mfma_f32_16x16x32_f16 v[54:57], v[152:155], v[46:49], v[54:57]
	v_mfma_f32_16x16x32_f16 v[74:77], v[152:155], v[176:179], v[74:77]
	v_mfma_f32_16x16x32_f16 v[90:93], v[152:155], v[180:183], v[90:93]
	v_mfma_f32_16x16x32_f16 v[62:65], v[152:155], v[228:231], v[62:65]
	s_waitcnt vmcnt(17)
	v_mfma_f32_16x16x32_f16 v[38:41], v[224:227], v[46:49], v[38:41]
	v_mfma_f32_16x16x32_f16 v[42:45], v[224:227], v[176:179], v[42:45]
	v_mfma_f32_16x16x32_f16 v[46:49], v[224:227], v[180:183], v[50:53]
	s_nop 2
	buffer_load_dwordx4 v[50:53], v147, s[16:19], s8 offen
	buffer_load_dwordx4 v[140:143], v148, s[16:19], s8 offen
	buffer_load_dwordx4 v[152:155], v149, s[16:19], s8 offen
	buffer_load_dwordx4 v[176:179], v150, s[16:19], s8 offen
	v_mfma_f32_16x16x32_f16 v[94:97], v[220:223], v[180:183], v[94:97]
	v_mfma_f32_16x16x32_f16 v[70:73], v[220:223], v[228:231], v[70:73]
	v_mfma_f32_16x16x32_f16 v[34:37], v[224:227], v[228:231], v[34:37]
	v_add_u32_e32 v100, s71, v100
	ds_read_b128 v[180:183], v100
	ds_read_b128 v[220:223], v100 offset:16384
	ds_read_b128 v[224:227], v100 offset:32768
	ds_read_b128 v[228:231], v100 offset:49152
	s_add_i32 s8, s22, s40
	s_waitcnt vmcnt(15) lgkmcnt(7)
	v_mfma_f32_16x16x32_f16 v[164:167], v[126:129], v[204:207], v[164:167]
	s_waitcnt lgkmcnt(6)
	v_mfma_f32_16x16x32_f16 v[168:171], v[126:129], v[208:211], v[168:171]
	s_waitcnt lgkmcnt(5)
	v_mfma_f32_16x16x32_f16 v[172:175], v[126:129], v[212:215], v[172:175]
	s_waitcnt lgkmcnt(4)
	v_mfma_f32_16x16x32_f16 v[82:85], v[126:129], v[216:219], v[82:85]
	s_waitcnt vmcnt(14)
	v_mfma_f32_16x16x32_f16 v[58:61], v[136:139], v[204:207], v[58:61]
	v_mfma_f32_16x16x32_f16 v[86:89], v[136:139], v[208:211], v[86:89]
	v_mfma_f32_16x16x32_f16 v[94:97], v[136:139], v[212:215], v[94:97]
	v_mfma_f32_16x16x32_f16 v[70:73], v[136:139], v[216:219], v[70:73]
	s_waitcnt vmcnt(13)
	v_mfma_f32_16x16x32_f16 v[54:57], v[184:187], v[204:207], v[54:57]
	v_mfma_f32_16x16x32_f16 v[74:77], v[184:187], v[208:211], v[74:77]
	v_mfma_f32_16x16x32_f16 v[90:93], v[184:187], v[212:215], v[90:93]
	v_mfma_f32_16x16x32_f16 v[62:65], v[184:187], v[216:219], v[62:65]
	s_waitcnt vmcnt(12)
	v_mfma_f32_16x16x32_f16 v[38:41], v[188:191], v[204:207], v[38:41]
	buffer_load_dwordx4 v[126:129], v147, s[16:19], s8 offen
	buffer_load_dwordx4 v[136:139], v148, s[16:19], s8 offen
	buffer_load_dwordx4 v[184:187], v149, s[16:19], s8 offen
	buffer_load_dwordx4 v[204:207], v150, s[16:19], s8 offen
	v_mfma_f32_16x16x32_f16 v[42:45], v[188:191], v[208:211], v[42:45]
	v_mfma_f32_16x16x32_f16 v[46:49], v[188:191], v[212:215], v[46:49]
	v_mfma_f32_16x16x32_f16 v[34:37], v[188:191], v[216:219], v[34:37]
	v_add_u32_e32 v111, s72, v111
	ds_read_b128 v[188:191], v111
	ds_read_b128 v[208:211], v111 offset:16384
	ds_read_b128 v[212:215], v111 offset:32768
	ds_read_b128 v[216:219], v111 offset:49152
	s_add_i32 s8, s22, s41
	s_waitcnt vmcnt(15) lgkmcnt(7)
	v_mfma_f32_16x16x32_f16 v[164:167], v[78:81], v[180:183], v[164:167]
	s_waitcnt lgkmcnt(6)
	v_mfma_f32_16x16x32_f16 v[168:171], v[78:81], v[220:223], v[168:171]
	s_waitcnt lgkmcnt(5)
	v_mfma_f32_16x16x32_f16 v[172:175], v[78:81], v[224:227], v[172:175]
	s_waitcnt lgkmcnt(4)
	v_mfma_f32_16x16x32_f16 v[78:81], v[78:81], v[228:231], v[82:85]
	s_waitcnt vmcnt(14)
	v_mfma_f32_16x16x32_f16 v[58:61], v[122:125], v[180:183], v[58:61]
	v_mfma_f32_16x16x32_f16 v[82:85], v[122:125], v[220:223], v[86:89]
	v_mfma_f32_16x16x32_f16 v[86:89], v[122:125], v[224:227], v[94:97]
	v_mfma_f32_16x16x32_f16 v[70:73], v[122:125], v[228:231], v[70:73]
	s_waitcnt vmcnt(13)
	v_mfma_f32_16x16x32_f16 v[54:57], v[156:159], v[180:183], v[54:57]
	v_mfma_f32_16x16x32_f16 v[74:77], v[156:159], v[220:223], v[74:77]
	v_mfma_f32_16x16x32_f16 v[90:93], v[156:159], v[224:227], v[90:93]
	v_mfma_f32_16x16x32_f16 v[62:65], v[156:159], v[228:231], v[62:65]
	s_waitcnt vmcnt(12)
	v_mfma_f32_16x16x32_f16 v[38:41], v[160:163], v[180:183], v[38:41]
	buffer_load_dwordx4 v[94:97], v147, s[16:19], s8 offen
	buffer_load_dwordx4 v[122:125], v148, s[16:19], s8 offen
	buffer_load_dwordx4 v[156:159], v149, s[16:19], s8 offen
	buffer_load_dwordx4 v[180:183], v150, s[16:19], s8 offen
	v_mfma_f32_16x16x32_f16 v[42:45], v[160:163], v[220:223], v[42:45]
	v_mfma_f32_16x16x32_f16 v[46:49], v[160:163], v[224:227], v[46:49]
	v_mfma_f32_16x16x32_f16 v[34:37], v[160:163], v[228:231], v[34:37]
	v_add_u32_e32 v98, s73, v98
	ds_read_b128 v[160:163], v98
	ds_read_b128 v[220:223], v98 offset:16384
	ds_read_b128 v[224:227], v98 offset:32768
	ds_read_b128 v[228:231], v98 offset:49152
	s_add_i32 s8, s22, s42
	s_waitcnt vmcnt(15) lgkmcnt(7)
	v_mfma_f32_16x16x32_f16 v[164:167], v[66:69], v[188:191], v[164:167]
	s_waitcnt lgkmcnt(6)
	v_mfma_f32_16x16x32_f16 v[168:171], v[66:69], v[208:211], v[168:171]
	s_waitcnt lgkmcnt(5)
	v_mfma_f32_16x16x32_f16 v[172:175], v[66:69], v[212:215], v[172:175]
	s_waitcnt lgkmcnt(4)
	v_mfma_f32_16x16x32_f16 v[66:69], v[66:69], v[216:219], v[78:81]
	s_waitcnt vmcnt(14)
	v_mfma_f32_16x16x32_f16 v[58:61], v[192:195], v[188:191], v[58:61]
	v_mfma_f32_16x16x32_f16 v[78:81], v[192:195], v[208:211], v[82:85]
	v_mfma_f32_16x16x32_f16 v[82:85], v[192:195], v[212:215], v[86:89]
	v_mfma_f32_16x16x32_f16 v[70:73], v[192:195], v[216:219], v[70:73]
	s_waitcnt vmcnt(13)
	v_mfma_f32_16x16x32_f16 v[54:57], v[196:199], v[188:191], v[54:57]
	v_mfma_f32_16x16x32_f16 v[74:77], v[196:199], v[208:211], v[74:77]
	v_mfma_f32_16x16x32_f16 v[86:89], v[196:199], v[212:215], v[90:93]
	v_mfma_f32_16x16x32_f16 v[62:65], v[196:199], v[216:219], v[62:65]
	s_waitcnt vmcnt(12)
	v_mfma_f32_16x16x32_f16 v[38:41], v[200:203], v[188:191], v[38:41]
	buffer_load_dwordx4 v[90:93], v147, s[16:19], s8 offen
	buffer_load_dwordx4 v[188:191], v148, s[16:19], s8 offen
	buffer_load_dwordx4 v[192:195], v149, s[16:19], s8 offen
	buffer_load_dwordx4 v[196:199], v150, s[16:19], s8 offen
	v_mfma_f32_16x16x32_f16 v[42:45], v[200:203], v[208:211], v[42:45]
	v_mfma_f32_16x16x32_f16 v[46:49], v[200:203], v[212:215], v[46:49]
	v_mfma_f32_16x16x32_f16 v[34:37], v[200:203], v[216:219], v[34:37]
	v_add_u32_e32 v99, s74, v99
	ds_read_b128 v[200:203], v99
	ds_read_b128 v[208:211], v99 offset:16384
	ds_read_b128 v[212:215], v99 offset:32768
	ds_read_b128 v[216:219], v99 offset:49152
	s_add_i32 s8, s22, s43
	s_waitcnt vmcnt(15) lgkmcnt(7)
	v_mfma_f32_16x16x32_f16 v[164:167], v[50:53], v[160:163], v[164:167]
	s_waitcnt lgkmcnt(6)
	v_mfma_f32_16x16x32_f16 v[168:171], v[50:53], v[220:223], v[168:171]
	s_waitcnt lgkmcnt(5)
	v_mfma_f32_16x16x32_f16 v[172:175], v[50:53], v[224:227], v[172:175]
	s_waitcnt lgkmcnt(4)
	v_mfma_f32_16x16x32_f16 v[50:53], v[50:53], v[228:231], v[66:69]
	s_waitcnt vmcnt(14)
	v_mfma_f32_16x16x32_f16 v[58:61], v[140:143], v[160:163], v[58:61]
	v_mfma_f32_16x16x32_f16 v[66:69], v[140:143], v[220:223], v[78:81]
	v_mfma_f32_16x16x32_f16 v[78:81], v[140:143], v[224:227], v[82:85]
	v_mfma_f32_16x16x32_f16 v[70:73], v[140:143], v[228:231], v[70:73]
	s_waitcnt vmcnt(13)
	v_mfma_f32_16x16x32_f16 v[54:57], v[152:155], v[160:163], v[54:57]
	v_mfma_f32_16x16x32_f16 v[74:77], v[152:155], v[220:223], v[74:77]
	v_mfma_f32_16x16x32_f16 v[82:85], v[152:155], v[224:227], v[86:89]
	v_mfma_f32_16x16x32_f16 v[62:65], v[152:155], v[228:231], v[62:65]
	s_waitcnt vmcnt(12)
	v_mfma_f32_16x16x32_f16 v[38:41], v[176:179], v[160:163], v[38:41]
	buffer_load_dwordx4 v[86:89], v147, s[16:19], s8 offen
	buffer_load_dwordx4 v[140:143], v148, s[16:19], s8 offen
	buffer_load_dwordx4 v[152:155], v149, s[16:19], s8 offen
	buffer_load_dwordx4 v[160:163], v150, s[16:19], s8 offen
	v_mfma_f32_16x16x32_f16 v[42:45], v[176:179], v[220:223], v[42:45]
	v_mfma_f32_16x16x32_f16 v[46:49], v[176:179], v[224:227], v[46:49]
	v_mfma_f32_16x16x32_f16 v[34:37], v[176:179], v[228:231], v[34:37]
	v_add_u32_e32 v100, s75, v100
	ds_read_b128 v[176:179], v100
	ds_read_b128 v[220:223], v100 offset:16384
	ds_read_b128 v[224:227], v100 offset:32768
	ds_read_b128 v[228:231], v100 offset:49152
	s_add_i32 s8, s22, s44
	s_waitcnt vmcnt(15) lgkmcnt(7)
	v_mfma_f32_16x16x32_f16 v[164:167], v[126:129], v[200:203], v[164:167]
	s_waitcnt lgkmcnt(6)
	v_mfma_f32_16x16x32_f16 v[168:171], v[126:129], v[208:211], v[168:171]
	s_waitcnt lgkmcnt(5)
	v_mfma_f32_16x16x32_f16 v[172:175], v[126:129], v[212:215], v[172:175]
	s_waitcnt lgkmcnt(4)
	v_mfma_f32_16x16x32_f16 v[50:53], v[126:129], v[216:219], v[50:53]
	s_waitcnt vmcnt(14)
	v_mfma_f32_16x16x32_f16 v[58:61], v[136:139], v[200:203], v[58:61]
	v_mfma_f32_16x16x32_f16 v[66:69], v[136:139], v[208:211], v[66:69]
	v_mfma_f32_16x16x32_f16 v[78:81], v[136:139], v[212:215], v[78:81]
	v_mfma_f32_16x16x32_f16 v[70:73], v[136:139], v[216:219], v[70:73]
	s_waitcnt vmcnt(13)
	v_mfma_f32_16x16x32_f16 v[54:57], v[184:187], v[200:203], v[54:57]
	v_mfma_f32_16x16x32_f16 v[74:77], v[184:187], v[208:211], v[74:77]
	v_mfma_f32_16x16x32_f16 v[82:85], v[184:187], v[212:215], v[82:85]
	v_mfma_f32_16x16x32_f16 v[62:65], v[184:187], v[216:219], v[62:65]
	s_waitcnt vmcnt(12)
	v_mfma_f32_16x16x32_f16 v[38:41], v[204:207], v[200:203], v[38:41]
	buffer_load_dwordx4 v[126:129], v147, s[16:19], s8 offen
	buffer_load_dwordx4 v[136:139], v148, s[16:19], s8 offen
	buffer_load_dwordx4 v[184:187], v149, s[16:19], s8 offen
	buffer_load_dwordx4 v[200:203], v150, s[16:19], s8 offen
	v_mfma_f32_16x16x32_f16 v[42:45], v[204:207], v[208:211], v[42:45]
	v_mfma_f32_16x16x32_f16 v[46:49], v[204:207], v[212:215], v[46:49]
	v_mfma_f32_16x16x32_f16 v[34:37], v[204:207], v[216:219], v[34:37]
	v_add_u32_e32 v111, s76, v111
	ds_read_b128 v[204:207], v111
	ds_read_b128 v[208:211], v111 offset:16384
	ds_read_b128 v[212:215], v111 offset:32768
	ds_read_b128 v[216:219], v111 offset:49152
	s_add_i32 s8, s22, s45
	s_waitcnt vmcnt(15) lgkmcnt(7)
	v_mfma_f32_16x16x32_f16 v[164:167], v[94:97], v[176:179], v[164:167]
	s_waitcnt lgkmcnt(6)
	v_mfma_f32_16x16x32_f16 v[168:171], v[94:97], v[220:223], v[168:171]
	s_waitcnt vmcnt(14)
	v_mfma_f32_16x16x32_f16 v[58:61], v[122:125], v[176:179], v[58:61]
	v_mfma_f32_16x16x32_f16 v[66:69], v[122:125], v[220:223], v[66:69]
	s_waitcnt lgkmcnt(5)
	v_mfma_f32_16x16x32_f16 v[78:81], v[122:125], v[224:227], v[78:81]
	s_waitcnt lgkmcnt(4)
	v_mfma_f32_16x16x32_f16 v[70:73], v[122:125], v[228:231], v[70:73]
	s_waitcnt vmcnt(13)
	v_mfma_f32_16x16x32_f16 v[54:57], v[156:159], v[176:179], v[54:57]
	v_mfma_f32_16x16x32_f16 v[74:77], v[156:159], v[220:223], v[74:77]
	v_mfma_f32_16x16x32_f16 v[82:85], v[156:159], v[224:227], v[82:85]
	v_mfma_f32_16x16x32_f16 v[62:65], v[156:159], v[228:231], v[62:65]
	s_waitcnt vmcnt(12)
	v_mfma_f32_16x16x32_f16 v[38:41], v[180:183], v[176:179], v[38:41]
	v_mfma_f32_16x16x32_f16 v[42:45], v[180:183], v[220:223], v[42:45]
	buffer_load_dwordx4 v[122:125], v147, s[16:19], s8 offen
	buffer_load_dwordx4 v[156:159], v148, s[16:19], s8 offen
	buffer_load_dwordx4 v[176:179], v149, s[16:19], s8 offen
	buffer_load_dwordx4 v[220:223], v150, s[16:19], s8 offen
	v_mfma_f32_16x16x32_f16 v[50:53], v[94:97], v[228:231], v[50:53]
	v_mfma_f32_16x16x32_f16 v[46:49], v[180:183], v[224:227], v[46:49]
	v_mfma_f32_16x16x32_f16 v[34:37], v[180:183], v[228:231], v[34:37]
	v_mfma_f32_16x16x32_f16 v[172:175], v[94:97], v[224:227], v[172:175]
	v_add_u32_e32 v98, s77, v98
	ds_read_b128 v[94:97], v98
	ds_read_b128 v[180:183], v98 offset:16384
	ds_read_b128 v[224:227], v98 offset:32768
	ds_read_b128 v[228:231], v98 offset:49152
	s_add_i32 s8, s22, s46
	s_waitcnt vmcnt(15) lgkmcnt(7)
	v_mfma_f32_16x16x32_f16 v[164:167], v[90:93], v[204:207], v[164:167]
	s_waitcnt lgkmcnt(6)
	v_mfma_f32_16x16x32_f16 v[168:171], v[90:93], v[208:211], v[168:171]
	s_waitcnt lgkmcnt(5)
	v_mfma_f32_16x16x32_f16 v[172:175], v[90:93], v[212:215], v[172:175]
	s_waitcnt lgkmcnt(4)
	v_mfma_f32_16x16x32_f16 v[90:93], v[90:93], v[216:219], v[50:53]
	s_waitcnt vmcnt(14)
	v_mfma_f32_16x16x32_f16 v[232:235], v[188:191], v[204:207], v[58:61]
	v_mfma_f32_16x16x32_f16 v[66:69], v[188:191], v[208:211], v[66:69]
	v_mfma_f32_16x16x32_f16 v[78:81], v[188:191], v[212:215], v[78:81]
	v_mfma_f32_16x16x32_f16 v[70:73], v[188:191], v[216:219], v[70:73]
	s_waitcnt vmcnt(13)
	v_mfma_f32_16x16x32_f16 v[188:191], v[192:195], v[204:207], v[54:57]
	v_mfma_f32_16x16x32_f16 v[74:77], v[192:195], v[208:211], v[74:77]
	v_mfma_f32_16x16x32_f16 v[82:85], v[192:195], v[212:215], v[82:85]
	v_mfma_f32_16x16x32_f16 v[62:65], v[192:195], v[216:219], v[62:65]
	s_waitcnt vmcnt(12)
	v_mfma_f32_16x16x32_f16 v[192:195], v[196:199], v[204:207], v[38:41]
	buffer_load_dwordx4 v[58:61], v147, s[16:19], s8 offen
	buffer_load_dwordx4 v[54:57], v148, s[16:19], s8 offen
	buffer_load_dwordx4 v[50:53], v149, s[16:19], s8 offen
	buffer_load_dwordx4 v[38:41], v150, s[16:19], s8 offen
	v_mfma_f32_16x16x32_f16 v[42:45], v[196:199], v[208:211], v[42:45]
	v_mfma_f32_16x16x32_f16 v[46:49], v[196:199], v[212:215], v[46:49]
	v_mfma_f32_16x16x32_f16 v[196:199], v[196:199], v[216:219], v[34:37]
	v_add_u32_e32 v99, s78, v99
	ds_read_b128 v[204:207], v99
	ds_read_b128 v[208:211], v99 offset:16384
	ds_read_b128 v[212:215], v99 offset:32768
	ds_read_b128 v[216:219], v99 offset:49152
	s_add_i32 s8, s22, s47
	s_waitcnt vmcnt(15) lgkmcnt(7)
	v_mfma_f32_16x16x32_f16 v[164:167], v[86:89], v[94:97], v[164:167]
	s_waitcnt lgkmcnt(6)
	v_mfma_f32_16x16x32_f16 v[168:171], v[86:89], v[180:183], v[168:171]
	s_waitcnt lgkmcnt(5)
	v_mfma_f32_16x16x32_f16 v[172:175], v[86:89], v[224:227], v[172:175]
	s_waitcnt lgkmcnt(4)
	v_mfma_f32_16x16x32_f16 v[86:89], v[86:89], v[228:231], v[90:93]
	s_waitcnt vmcnt(14)
	v_mfma_f32_16x16x32_f16 v[232:235], v[140:143], v[94:97], v[232:235]
	v_mfma_f32_16x16x32_f16 v[66:69], v[140:143], v[180:183], v[66:69]
	v_mfma_f32_16x16x32_f16 v[236:239], v[140:143], v[224:227], v[78:81]
	v_mfma_f32_16x16x32_f16 v[70:73], v[140:143], v[228:231], v[70:73]
	s_waitcnt vmcnt(13)
	v_mfma_f32_16x16x32_f16 v[140:143], v[152:155], v[94:97], v[188:191]
	v_mfma_f32_16x16x32_f16 v[74:77], v[152:155], v[180:183], v[74:77]
	v_mfma_f32_16x16x32_f16 v[82:85], v[152:155], v[224:227], v[82:85]
	v_mfma_f32_16x16x32_f16 v[62:65], v[152:155], v[228:231], v[62:65]
	s_waitcnt vmcnt(12)
	v_mfma_f32_16x16x32_f16 v[152:155], v[160:163], v[94:97], v[192:195]
	buffer_load_dwordx4 v[94:97], v147, s[16:19], s8 offen
	buffer_load_dwordx4 v[90:93], v148, s[16:19], s8 offen
	buffer_load_dwordx4 v[78:81], v149, s[16:19], s8 offen
	buffer_load_dwordx4 v[34:37], v150, s[16:19], s8 offen
	v_mfma_f32_16x16x32_f16 v[42:45], v[160:163], v[180:183], v[42:45]
	v_mfma_f32_16x16x32_f16 v[46:49], v[160:163], v[224:227], v[46:49]
	v_mfma_f32_16x16x32_f16 v[160:163], v[160:163], v[228:231], v[196:199]
	v_add_u32_e32 v100, s79, v100
	ds_read_b128 v[180:183], v100
	ds_read_b128 v[188:191], v100 offset:16384
	ds_read_b128 v[192:195], v100 offset:32768
	ds_read_b128 v[196:199], v100 offset:49152
	s_add_i32 s8, s22, s48
	s_waitcnt vmcnt(15) lgkmcnt(7)
	v_mfma_f32_16x16x32_f16 v[164:167], v[126:129], v[204:207], v[164:167]
	s_waitcnt lgkmcnt(6)
	v_mfma_f32_16x16x32_f16 v[168:171], v[126:129], v[208:211], v[168:171]
	s_waitcnt lgkmcnt(5)
	v_mfma_f32_16x16x32_f16 v[172:175], v[126:129], v[212:215], v[172:175]
	s_waitcnt lgkmcnt(4)
	v_mfma_f32_16x16x32_f16 v[86:89], v[126:129], v[216:219], v[86:89]
	s_waitcnt vmcnt(14)
	v_mfma_f32_16x16x32_f16 v[126:129], v[136:139], v[204:207], v[232:235]
	v_mfma_f32_16x16x32_f16 v[66:69], v[136:139], v[208:211], v[66:69]
	v_mfma_f32_16x16x32_f16 v[224:227], v[136:139], v[212:215], v[236:239]
	v_mfma_f32_16x16x32_f16 v[136:139], v[136:139], v[216:219], v[70:73]
	s_waitcnt vmcnt(13)
	v_mfma_f32_16x16x32_f16 v[140:143], v[184:187], v[204:207], v[140:143]
	v_mfma_f32_16x16x32_f16 v[74:77], v[184:187], v[208:211], v[74:77]
	v_mfma_f32_16x16x32_f16 v[228:231], v[184:187], v[212:215], v[82:85]
	v_mfma_f32_16x16x32_f16 v[184:187], v[184:187], v[216:219], v[62:65]
	s_waitcnt vmcnt(12)
	v_mfma_f32_16x16x32_f16 v[152:155], v[200:203], v[204:207], v[152:155]
	v_mfma_f32_16x16x32_f16 v[204:207], v[200:203], v[208:211], v[42:45]
	buffer_load_dwordx4 v[82:85], v147, s[16:19], s8 offen
	buffer_load_dwordx4 v[70:73], v148, s[16:19], s8 offen
	buffer_load_dwordx4 v[62:65], v149, s[16:19], s8 offen
	buffer_load_dwordx4 v[42:45], v150, s[16:19], s8 offen
	v_mfma_f32_16x16x32_f16 v[46:49], v[200:203], v[212:215], v[46:49]
	v_mfma_f32_16x16x32_f16 v[160:163], v[200:203], v[216:219], v[160:163]
	v_add_u32_e32 v0, 0x1ac00, v104
	ds_read_b128 v[240:243], v0
	ds_read_b128 v[244:247], v0 offset:16
	s_waitcnt vmcnt(12) lgkmcnt(5)
	v_mfma_f32_16x16x32_f16 v[164:167], v[122:125], v[180:183], v[164:167]
	v_mfma_f32_16x16x32_f16 v[126:129], v[156:159], v[180:183], v[126:129]
	v_mfma_f32_16x16x32_f16 v[140:143], v[176:179], v[180:183], v[140:143]
	v_mfma_f32_16x16x32_f16 v[152:155], v[220:223], v[180:183], v[152:155]
	s_waitcnt lgkmcnt(4)
	v_mfma_f32_16x16x32_f16 v[168:171], v[122:125], v[188:191], v[168:171]
	v_mfma_f32_16x16x32_f16 v[208:211], v[156:159], v[188:191], v[66:69]
	v_mfma_f32_16x16x32_f16 v[212:215], v[176:179], v[188:191], v[74:77]
	v_mfma_f32_16x16x32_f16 v[204:207], v[220:223], v[188:191], v[204:207]
	s_waitcnt lgkmcnt(3)
	v_mfma_f32_16x16x32_f16 v[172:175], v[122:125], v[192:195], v[172:175]
	v_cvt_pk_f16_f32 v232, v164, v165
	v_cvt_pk_f16_f32 v233, v166, v167
	v_pk_max_f16 v232, v232, 0
	v_pk_max_f16 v233, v233, 0
	v_mfma_f32_16x16x32_f16 v[224:227], v[156:159], v[192:195], v[224:227]
	v_cvt_pk_f16_f32 v234, v126, v127
	v_cvt_pk_f16_f32 v235, v128, v129
	v_pk_max_f16 v234, v234, 0
	v_pk_max_f16 v235, v235, 0
	v_mfma_f32_16x16x32_f16 v[228:231], v[176:179], v[192:195], v[228:231]
	v_cvt_pk_f16_f32 v236, v140, v141
	v_cvt_pk_f16_f32 v237, v142, v143
	v_pk_max_f16 v236, v236, 0
	v_pk_max_f16 v237, v237, 0
	v_mfma_f32_16x16x32_f16 v[216:219], v[220:223], v[192:195], v[46:49]
	v_cvt_pk_f16_f32 v238, v152, v153
	v_cvt_pk_f16_f32 v239, v154, v155
	v_pk_max_f16 v238, v238, 0
	v_pk_max_f16 v239, v239, 0
	s_waitcnt lgkmcnt(2)
	v_mfma_f32_16x16x32_f16 v[200:203], v[122:125], v[196:199], v[86:89]
	v_cvt_pk_f16_f32 v180, v168, v169
	v_cvt_pk_f16_f32 v181, v170, v171
	v_pk_max_f16 v180, v180, 0
	v_pk_max_f16 v181, v181, 0
	s_add_i32 s8, s22, s49
	buffer_load_dwordx4 v[86:89], v147, s[16:19], s8 offen
	buffer_load_dwordx4 v[74:77], v148, s[16:19], s8 offen
	buffer_load_dwordx4 v[66:69], v149, s[16:19], s8 offen
	buffer_load_dwordx4 v[46:49], v150, s[16:19], s8 offen
	v_mfma_f32_16x16x32_f16 v[136:139], v[156:159], v[196:199], v[136:139]
	v_cvt_pk_f16_f32 v182, v208, v209
	v_cvt_pk_f16_f32 v183, v210, v211
	v_pk_max_f16 v182, v182, 0
	v_pk_max_f16 v183, v183, 0
	s_waitcnt lgkmcnt(1)
	v_mfma_f32_16x16x32_f16 v[252:255], v[240:243], v[232:235], 0
	v_cvt_pk_f16_f32 v232, v172, v173
	v_cvt_pk_f16_f32 v233, v174, v175
	v_pk_max_f16 v232, v232, 0
	v_pk_max_f16 v233, v233, 0
	v_mfma_f32_16x16x32_f16 v[184:187], v[176:179], v[196:199], v[184:187]
	v_cvt_pk_f16_f32 v188, v212, v213
	v_cvt_pk_f16_f32 v189, v214, v215
	v_pk_max_f16 v188, v188, 0
	v_pk_max_f16 v189, v189, 0
	s_waitcnt lgkmcnt(0)
	v_mfma_f32_16x16x32_f16 v[252:255], v[244:247], v[236:239], v[252:255]
	ds_read_u16 v102, v114
	ds_read_u16 v103, v114 offset:512
	ds_read_u16 v115, v114 offset:1024
	ds_read_u16 v116, v114 offset:1536
	v_cvt_pk_f16_f32 v234, v224, v225
	v_cvt_pk_f16_f32 v235, v226, v227
	v_pk_max_f16 v234, v234, 0
	v_pk_max_f16 v235, v235, 0
	v_mfma_f32_16x16x32_f16 v[160:163], v[220:223], v[196:199], v[160:163]
	v_cvt_pk_f16_f32 v190, v204, v205
	v_cvt_pk_f16_f32 v191, v206, v207
	v_pk_max_f16 v190, v190, 0
	v_pk_max_f16 v191, v191, 0
	v_mfma_f32_16x16x32_f16 v[192:195], v[240:243], v[180:183], 0
	v_cvt_pk_f16_f32 v236, v228, v229
	v_cvt_pk_f16_f32 v237, v230, v231
	v_pk_max_f16 v236, v236, 0
	v_pk_max_f16 v237, v237, 0
	v_mfma_f32_16x16x32_f16 v[192:195], v[244:247], v[188:191], v[192:195]
	v_cvt_pk_f16_f32 v238, v216, v217
	v_cvt_pk_f16_f32 v239, v218, v219
	v_pk_max_f16 v238, v238, 0
	v_pk_max_f16 v239, v239, 0
	v_cvt_pk_f16_f32 v180, v200, v201
	v_cvt_pk_f16_f32 v181, v202, v203
	v_pk_max_f16 v180, v180, 0
	v_pk_max_f16 v181, v181, 0
	v_mfma_f32_16x16x32_f16 v[196:199], v[240:243], v[232:235], 0
	v_cvt_pk_f16_f32 v182, v136, v137
	v_cvt_pk_f16_f32 v183, v138, v139
	v_pk_max_f16 v182, v182, 0
	v_pk_max_f16 v183, v183, 0
	v_mfma_f32_16x16x32_f16 v[196:199], v[244:247], v[236:239], v[196:199]
	v_cvt_pk_f16_f32 v188, v184, v185
	v_cvt_pk_f16_f32 v189, v186, v187
	v_pk_max_f16 v188, v188, 0
	v_pk_max_f16 v189, v189, 0
	v_cvt_pk_f16_f32 v190, v160, v161
	v_cvt_pk_f16_f32 v191, v162, v163
	v_pk_max_f16 v190, v190, 0
	v_pk_max_f16 v191, v191, 0
	v_mfma_f32_16x16x32_f16 v[122:125], v[240:243], v[180:183], 0
	s_nop 0
	v_mfma_f32_16x16x32_f16 v[122:125], v[244:247], v[188:191], v[122:125]
	v_add_u32_e32 v145, 0x12c00, v105
	ds_read_b128 v[240:243], v145 offset:2048
	ds_read_b128 v[244:247], v145 offset:2064
	ds_read_b128 v[248:251], v145 offset:2080
	s_load_dword s30, s[12:13], 0x0
	v_cndmask_b32_e64 v0, v252, v192, s[2:3]
	ds_read_b128 v[252:255], v145 offset:2096
	v_cndmask_b32_e64 v0, v0, v196, s[0:1]
	v_cndmask_b32_e64 v0, v0, v122, s[26:27]
	ds_write_b32 v112, v0
	s_waitcnt vmcnt(16)
	v_cndmask_b32_e64 v1, v30, v134, s[0:1]
	v_bfi_b32 v30, s10, v1, v30
	v_perm_b32 v1, v22, v134, s24
	v_cndmask_b32_e64 v22, v22, v1, s[0:1]
	v_bfi_b32 v1, s10, v135, v18
	v_perm_b32 v121, v10, v135, s24
	v_cndmask_b32_e64 v18, v18, v1, s[0:1]
	v_cndmask_b32_e64 v10, v10, v121, s[0:1]
	s_add_i32 s22, s22, 0x80000
	s_add_i32 s11, s11, 1
	s_add_u32 s12, s12, 4
	s_addc_u32 s13, s13, 0
	v_add_u32_e32 v104, v109, v104
	v_add_u32_e32 v105, 0x800, v105
	v_add_u32_e32 v114, 2, v114
	s_cmp_eq_u32 s22, 0x898000
	s_waitcnt lgkmcnt(0)
	s_barrier
	ds_read_b128 v[232:235], v113
	ds_read_b128 v[236:239], v113 offset:1024
	s_waitcnt lgkmcnt(0)
	v_add_f32_e32 v0, v232, v233
	v_add_f32_e32 v1, v234, v235
	v_add_f32_e32 v121, v236, v237
	v_add_f32_e32 v144, v238, v239
	v_add_f32_e32 v0, v0, v1
	v_add_f32_e32 v121, v121, v144
	v_add_f32_e32 v0, v0, v121
	v_add_f32_e32 v0, s30, v0
	ds_write_b32 v106, v0
	v_cvt_f16_f32_e32 v1, v0
	v_cvt_f16_f32_e32 v121, v0
	s_nop 1
	v_permlane16_swap_b32_e32 v1, v121
	v_mov_b32_e32 v144, v1
	v_mov_b32_e32 v145, v121
	s_nop 1
	v_permlane32_swap_b32_e32 v1, v144
	v_permlane32_swap_b32_e32 v121, v145
	v_add_u32_e32 v106, 4, v106
	s_cbranch_scc0 .LBB1_4
